# v39 + P9 (dispatch) stores write-through (sc1) and no L2 write-back fence at the barrier that follows it
# baseline (speedup 1.0000x reference)
.LBB0_1517:
	v_or_b32_e32 v44, s73, v1
	v_or_b32_e32 v45, s72, v2
	s_add_i32 s13, s72, 2
	s_add_i32 s12, s73, 2
	s_add_i32 s14, s73, 4
	s_add_i32 s15, s72, 4
	s_add_i32 s16, s73, 6
	s_add_i32 s18, s73, 8
	s_add_i32 s20, s73, 10
	s_add_i32 s22, s73, 12
	s_add_i32 s24, s73, 14
	v_lshlrev_b32_e32 v4, 6, v44
	v_lshlrev_b32_e32 v26, 6, v45
	v_or_b32_e32 v47, s13, v2
	s_add_i32 s17, s72, 6
	v_or_b32_e32 v46, s12, v1
	v_or_b32_e32 v48, s14, v1
	v_or_b32_e32 v49, s15, v2
	v_or_b32_e32 v50, s16, v1
	v_or_b32_e32 v52, s18, v1
	v_or_b32_e32 v54, s20, v1
	v_or_b32_e32 v56, s22, v1
	v_or_b32_e32 v58, s24, v1
	v_or_b32_e32 v24, v4, v3
	v_or_b32_e32 v4, v26, v196
	v_lshlrev_b32_e32 v28, 6, v47
	v_mov_b32_e32 v25, v5
	s_add_i32 s19, s72, 8
	v_or_b32_e32 v51, s17, v2
	v_lshlrev_b32_e32 v26, 6, v46
	v_lshlrev_b32_e32 v30, 6, v48
	v_lshlrev_b32_e32 v60, 6, v49
	v_lshlrev_b32_e32 v32, 6, v50
	v_lshlrev_b32_e32 v34, 6, v52
	v_lshlrev_b32_e32 v36, 6, v54
	v_lshlrev_b32_e32 v38, 6, v56
	v_lshlrev_b32_e32 v42, 6, v58
	v_lshl_add_u64 v[40:41], v[4:5], 2, s[54:55]
	v_or_b32_e32 v4, v28, v196
	v_mov_b32_e32 v27, v5
	s_add_i32 s21, s72, 10
	v_or_b32_e32 v53, s19, v2
	v_lshlrev_b32_e32 v61, 6, v51
	v_lshl_add_u64 v[24:25], v[24:25], 2, s[54:55]
	v_or_b32_e32 v26, v26, v3
	v_or_b32_e32 v28, v30, v3
	v_or_b32_e32 v30, v32, v3
	v_or_b32_e32 v32, v34, v3
	v_or_b32_e32 v34, v36, v3
	v_or_b32_e32 v36, v38, v3
	v_or_b32_e32 v38, v42, v3
	v_lshl_add_u64 v[42:43], v[4:5], 2, s[54:55]
	v_or_b32_e32 v4, v60, v196
	v_mov_b32_e32 v29, v5
	v_mov_b32_e32 v31, v5
	s_add_i32 s23, s72, 12
	v_or_b32_e32 v55, s21, v2
	v_lshlrev_b32_e32 v62, 6, v53
	v_lshl_add_u64 v[26:27], v[26:27], 2, s[54:55]
	global_load_dword v60, v[24:25], off
	s_nop 0
	global_load_dword v40, v[40:41], off
	s_nop 0
	global_load_dword v41, v[42:43], off
	s_nop 0
	global_load_dword v42, v[26:27], off
	v_lshl_add_u64 v[24:25], v[4:5], 2, s[54:55]
	v_or_b32_e32 v4, v61, v196
	s_add_i32 s25, s72, 14
	v_or_b32_e32 v57, s23, v2
	v_lshlrev_b32_e32 v63, 6, v55
	v_lshl_add_u64 v[28:29], v[28:29], 2, s[54:55]
	v_lshl_add_u64 v[30:31], v[30:31], 2, s[54:55]
	v_lshl_add_u64 v[26:27], v[4:5], 2, s[54:55]
	v_or_b32_e32 v4, v62, v196
	v_mov_b32_e32 v33, v5
	v_mov_b32_e32 v35, v5
	v_or_b32_e32 v59, s25, v2
	v_lshlrev_b32_e32 v64, 6, v57
	global_load_dword v43, v[24:25], off
	s_nop 0
	global_load_dword v28, v[28:29], off
	s_nop 0
	global_load_dword v29, v[30:31], off
	s_nop 0
	global_load_dword v30, v[26:27], off
	v_lshl_add_u64 v[24:25], v[4:5], 2, s[54:55]
	v_or_b32_e32 v4, v63, v196
	v_lshlrev_b32_e32 v65, 6, v59
	v_lshl_add_u64 v[32:33], v[32:33], 2, s[54:55]
	v_lshl_add_u64 v[34:35], v[34:35], 2, s[54:55]
	v_lshl_add_u64 v[26:27], v[4:5], 2, s[54:55]
	v_or_b32_e32 v4, v64, v196
	global_load_dword v31, v[32:33], off
	s_nop 0
	global_load_dword v32, v[24:25], off
	global_load_dword v33, v[26:27], off
	s_nop 0
	global_load_dword v34, v[34:35], off
	v_lshl_add_u64 v[24:25], v[4:5], 2, s[54:55]
	v_or_b32_e32 v4, v65, v196
	v_mov_b32_e32 v37, v5
	v_mov_b32_e32 v39, v5
	v_lshl_add_u64 v[26:27], v[4:5], 2, s[54:55]
	v_lshl_add_u64 v[36:37], v[36:37], 2, s[54:55]
	v_lshl_add_u64 v[38:39], v[38:39], 2, s[54:55]
	global_load_dword v4, v[24:25], off
	s_nop 0
	global_load_dword v24, v[36:37], off
	global_load_dword v25, v[38:39], off
	s_nop 0
	global_load_dword v26, v[26:27], off
	v_cmp_gt_i32_e64 s[12:13], s69, v45
	v_cmp_gt_i32_e64 s[14:15], s70, v44
	v_cmp_gt_i32_e64 s[16:17], s69, v47
	v_cmp_gt_i32_e64 s[18:19], s70, v46
	v_cmp_gt_i32_e64 s[20:21], s70, v48
	v_cmp_gt_i32_e64 s[22:23], s69, v49
	v_cmp_gt_i32_e64 s[24:25], s70, v50
	v_cmp_gt_i32_e64 s[26:27], s69, v51
	v_cmp_gt_i32_e64 s[28:29], s69, v53
	v_cmp_gt_i32_e64 s[30:31], s70, v52
	v_cmp_gt_i32_e64 s[34:35], s69, v55
	v_cmp_gt_i32_e64 s[36:37], s70, v54
	v_cmp_gt_i32_e64 s[38:39], s70, v56
	v_cmp_gt_i32_e64 s[40:41], s69, v57
	v_cmp_gt_i32_e64 s[42:43], s70, v58
	v_cmp_gt_i32_e64 s[44:45], s69, v59
	s_add_i32 s72, s72, 16
	s_add_i32 s73, s73, 16
	s_add_i32 s71, s71, -16
	s_cmp_lg_u32 s71, 0
	s_waitcnt vmcnt(15)
	v_cndmask_b32_e64 v27, 0, v60, s[14:15]
	s_waitcnt vmcnt(14)
	v_cndmask_b32_e64 v35, 0, v40, s[12:13]
	s_waitcnt vmcnt(13)
	v_add3_u32 v23, v40, v23, v41
	s_waitcnt vmcnt(12)
	v_add3_u32 v13, v60, v13, v42
	v_cndmask_b32_e64 v36, 0, v42, s[18:19]
	v_cndmask_b32_e64 v37, 0, v41, s[16:17]
	v_add3_u32 v12, v35, v12, v37
	v_add3_u32 v10, v27, v10, v36
	s_waitcnt vmcnt(11)
	v_cndmask_b32_e64 v27, 0, v43, s[22:23]
	s_waitcnt vmcnt(10)
	v_cndmask_b32_e64 v35, 0, v28, s[20:21]
	s_waitcnt vmcnt(9)
	v_add3_u32 v13, v28, v13, v29
	s_waitcnt vmcnt(8)
	v_add3_u32 v23, v43, v23, v30
	v_cndmask_b32_e64 v28, 0, v30, s[26:27]
	v_cndmask_b32_e64 v29, 0, v29, s[24:25]
	v_add3_u32 v10, v35, v10, v29
	v_add3_u32 v12, v27, v12, v28
	s_waitcnt vmcnt(7)
	v_cndmask_b32_e64 v27, 0, v31, s[30:31]
	s_waitcnt vmcnt(6)
	v_cndmask_b32_e64 v28, 0, v32, s[28:29]
	s_waitcnt vmcnt(5)
	v_add3_u32 v23, v32, v23, v33
	s_waitcnt vmcnt(4)
	v_add3_u32 v13, v31, v13, v34
	v_cndmask_b32_e64 v29, 0, v34, s[36:37]
	v_cndmask_b32_e64 v30, 0, v33, s[34:35]
	v_add3_u32 v12, v28, v12, v30
	v_add3_u32 v10, v27, v10, v29
	s_waitcnt vmcnt(3)
	v_cndmask_b32_e64 v27, 0, v4, s[40:41]
	s_waitcnt vmcnt(2)
	v_cndmask_b32_e64 v28, 0, v24, s[38:39]
	s_waitcnt vmcnt(1)
	v_add3_u32 v13, v24, v13, v25
	s_waitcnt vmcnt(0)
	v_add3_u32 v23, v4, v23, v26
	v_cndmask_b32_e64 v4, 0, v26, s[44:45]
	v_cndmask_b32_e64 v24, 0, v25, s[42:43]
	v_add3_u32 v10, v28, v10, v24
	v_add3_u32 v12, v27, v12, v4
	s_cbranch_scc1 .LBB0_1517
	v_add_u32_e32 v4, v23, v13
	v_add_u32_e32 v10, v12, v10
	ds_write2st64_b32 v8, v10, v4 offset1:8
	s_waitcnt lgkmcnt(0)
	s_barrier
	s_mov_b64 s[14:15], exec
	v_readlane_b32 s12, v254, 4
	v_readlane_b32 s13, v254, 5
	s_and_b64 s[12:13], s[14:15], s[12:13]
	s_mov_b64 exec, s[12:13]
	s_cbranch_execz .LBB0_1536
	ds_read2st64_b32 v[12:13], v8 offset1:1
	ds_read2st64_b32 v[24:25], v8 offset0:8 offset1:9
	ds_read2st64_b32 v[26:27], v8 offset0:2 offset1:3
	ds_read2st64_b32 v[28:29], v8 offset0:4 offset1:5
	ds_read2st64_b32 v[30:31], v8 offset0:6 offset1:7
	s_waitcnt lgkmcnt(4)
	v_add_u32_e32 v4, v13, v12
	ds_read2st64_b32 v[12:13], v8 offset0:10 offset1:11
	ds_read2st64_b32 v[32:33], v8 offset0:12 offset1:13
	ds_read2st64_b32 v[34:35], v8 offset0:14 offset1:15
	s_waitcnt lgkmcnt(6)
	v_add_u32_e32 v10, v25, v24
	s_waitcnt lgkmcnt(5)
	v_add3_u32 v4, v4, v26, v27
	s_waitcnt lgkmcnt(2)
	v_add3_u32 v10, v10, v12, v13
	v_add3_u32 v4, v4, v28, v29
	s_waitcnt lgkmcnt(1)
	v_add3_u32 v10, v10, v32, v33
	v_add3_u32 v12, v4, v30, v31
	s_waitcnt lgkmcnt(0)
	v_add3_u32 v4, v10, v34, v35
	s_cmp_lg_u32 s69, 0
	ds_write_b32 v8, v12 offset:4096
	s_cbranch_scc1 .LBB0_1521
	global_store_dword v[6:7], v4, off sc1

.LBB0_1536:
	s_or_b64 exec, exec, s[14:15]
	s_waitcnt lgkmcnt(0)
	s_barrier
	s_and_saveexec_b64 s[12:13], vcc
	s_cbranch_execz .LBB0_1515
	v_lshl_or_b32 v12, s69, 8, v0
	v_ashrrev_i32_e32 v13, 31, v12
	v_lshlrev_b64 v[24:25], 2, v[12:13]
	v_lshl_add_u64 v[26:27], s[56:57], 0, v[24:25]
	global_load_dword v4, v[26:27], off
	v_lshl_add_u64 v[26:27], s[58:59], 0, v[24:25]
	global_load_dword v10, v[26:27], off
	v_lshl_add_u64 v[26:27], s[60:61], 0, v[24:25]
	global_load_dword v23, v[26:27], off
	v_ashrrev_i32_e32 v30, 3, v12
	s_waitcnt vmcnt(2)
	v_lshl_add_u32 v4, v4, 2, 0
	v_add_u32_e32 v13, 0x20b20, v4
	ds_read_b32 v26, v13
	ds_read_b32 v4, v4 offset:4096
	v_lshl_add_u64 v[12:13], s[62:63], 0, v[24:25]
	s_waitcnt vmcnt(1) lgkmcnt(0)
	v_add3_u32 v24, v4, v26, v10
	v_ashrrev_i32_e32 v25, 31, v24
	v_lshlrev_b64 v[26:27], 2, v[24:25]
	v_lshl_add_u64 v[28:29], s[64:65], 0, v[26:27]
	v_lshl_add_u64 v[26:27], s[66:67], 0, v[26:27]
	global_store_dword v[28:29], v30, off sc1
	s_waitcnt vmcnt(1)
	global_store_dword v[26:27], v23, off sc1
	global_store_dword v[12:13], v24, off sc1
	s_branch .LBB0_1515

.LBB0_1571:
	s_andn2_saveexec_b64 s[6:7], s[6:7]
	s_cbranch_execz .LBB0_1591
	s_mov_b64 s[6:7], exec
	s_waitcnt lgkmcnt(0)
	s_waitcnt vmcnt(0)
	v_mbcnt_lo_u32_b32 v2, s6, 0
	v_mbcnt_hi_u32_b32 v2, s7, v2
	v_cmp_eq_u32_e32 vcc, 0, v2
	s_and_saveexec_b64 s[8:9], vcc
	s_cbranch_execz .LBB0_1574
	s_bcnt1_i32_b64 s6, s[6:7]
	v_mov_b32_e32 v3, 0x7000
	v_mov_b32_e32 v4, s6
	global_atomic_add v3, v3, v4, s[50:51] offset:1024 sc0
